# v023 but GEMM-in epilogues: full-WG tile conversion on units 0,1 (gelu), half-WG on units 2..7 (1000 tiles), dedicated 5912
# speedup vs baseline: 1.0054x; 1.0007x over previous
.LBB0_86:
	s_cmp_lt_i32 s50, 2
	s_cselect_b64 s[6:7], -1, 0
	s_and_b64 s[0:1], s[6:7], s[2:3]
	s_andn2_b64 vcc, exec, s[0:1]
	v_writelane_b32 v254, s60, 4
	s_cbranch_vccnz .LBB0_260
	s_mov_b64 s[2:3], s[80:81]
	s_load_dwordx2 s[8:9], s[2:3], 0xa8
	s_cmpk_lg_i32 s56, 0x100
	s_cselect_b32 s0, s56, 0xc8
	s_cmp_ge_i32 s78, s0
	s_mov_b64 s[4:5], -1
	s_cbranch_scc0 .LBB0_145
	s_sub_i32 s1, s78, s0
	s_cmpk_gt_i32 s1, 0x1717
	s_cbranch_scc1 .LBB0_144
	s_sub_i32 s20, s56, s0
	s_abs_i32 s4, s20
	v_cvt_f32_u32_e32 v1, s4
	s_load_dwordx2 s[10:11], s[2:3], 0x78
	s_load_dwordx2 s[12:13], s[2:3], 0x88
	s_sub_i32 s2, s20, s1
	s_add_i32 s3, s2, 0x1717
	v_rcp_iflag_f32_e32 v1, v1
	s_sub_i32 s2, 0xffffe8e9, s2
	s_xor_b32 s14, s3, s20
	s_sub_i32 s5, 0, s4
	v_mul_f32_e32 v1, 0x4f7ffffe, v1
	v_cvt_u32_f32_e32 v1, v1
	s_max_i32 s2, s3, s2
	s_ashr_i32 s3, s14, 31
	v_readfirstlane_b32 s14, v1
	s_mul_i32 s5, s5, s14
	s_mul_hi_u32 s5, s14, s5
	s_add_i32 s14, s14, s5
	s_mul_hi_u32 s5, s2, s14
	s_mul_i32 s14, s5, s4
	s_sub_i32 s2, s2, s14
	s_add_i32 s14, s5, 1
	s_sub_i32 s15, s2, s4
	s_cmp_ge_u32 s2, s4
	s_cselect_b32 s5, s14, s5
	s_cselect_b32 s2, s15, s2
	s_add_i32 s14, s5, 1
	s_cmp_ge_u32 s2, s4
	s_cselect_b32 s2, s14, s5
	s_xor_b32 s2, s2, s3
	s_sub_i32 s29, s2, s3
	s_lshl_b32 s21, s29, 2
	s_add_i32 s22, s21, -1
	s_cmp_gt_i32 s29, 0
	s_cselect_b64 s[2:3], -1, 0
	s_and_b64 s[4:5], s[2:3], exec
	s_cselect_b32 s18, 0, s22
	s_ashr_i32 s4, s18, 2
	s_mul_i32 s17, s4, s20
	s_add_i32 s17, s17, s1
	s_cmpk_gt_i32 s17, 0x1fff
	s_mov_b32 s5, 0
	s_cbranch_scc0 .LBB0_91
	s_add_i32 s4, s17, 0xffffe000
	s_lshr_b32 s4, s4, 7
	s_lshl_b64 s[4:5], s[4:5], 24
	s_waitcnt lgkmcnt(0)
	s_add_u32 s14, s12, s4
	s_addc_u32 s15, s13, s5
	s_lshl_b32 s4, s17, 4
	s_and_b32 s26, s4, 0x780
	s_lshl_b32 s4, s17, 8
	s_and_b32 s16, s4, 0x700
	s_mov_b64 s[4:5], 0x800
	s_cbranch_execz .LBB0_92
	s_branch .LBB0_93

.LBB0_160:
	s_add_i32 s89, s59, -1
	s_cmp_lt_u32 s89, 8
	s_cselect_b32 s88, 1, 0
	s_cbranch_scc0 .Lp1c_skip1
	s_cmp_lt_u32 s89, 2
	s_cbranch_scc1 .Lp1c_full
	s_and_b32 s90, s89, 1
	s_lshr_b32 s91, s57, 2
	s_cmp_eq_u32 s90, s91
	s_cselect_b32 s88, 1, 0
	s_cbranch_scc0 .Lp1c_skip1
	s_lshr_b32 s89, s89, 1
	s_add_u32 s89, s89, 1
.Lp1c_full:
	s_mul_i32 s89, s89, 200
	s_add_u32 s89, s89, s78
	s_add_u32 s89, s89, 5912
	s_cmp_lt_u32 s89, 0x2000
	s_cselect_b32 s88, 1, 0
	s_cbranch_scc0 .Lp1c_skip1
	s_lshr_b32 s90, s89, 4
	s_lshl_b32 s90, s90, 21
	s_and_b32 s91, s89, 15
	s_lshl_b32 s92, s91, 10
	s_or_b32 s90, s90, s92
	s_lshl_b32 s92, s57, 7
	s_or_b32 s90, s90, s92
	s_add_u32 s84, s82, s90
	s_addc_u32 s85, s83, 0
	s_lshr_b32 s90, s89, 8
	s_lshl_b32 s90, s90, 23
	s_lshl_b32 s91, s91, 19
	s_or_b32 s90, s90, s91
	s_bfe_u32 s91, s89, 0x40004
	s_lshl_b32 s91, s91, 7
	s_or_b32 s90, s90, s91
	s_lshl_b32 s91, s57, 15
	s_or_b32 s90, s90, s91
	s_add_u32 s90, s90, 0x4ee00000
	s_add_u32 s86, s48, s90
	s_addc_u32 s87, s49, 0
	global_load_dwordx4 v[180:183], v245, s[84:85] nt
	s_add_u32 s84, s84, 0x4000
	s_addc_u32 s85, s85, 0
	global_load_dwordx4 v[184:187], v245, s[84:85] nt
	s_add_u32 s84, s84, 0x4000
	s_addc_u32 s85, s85, 0
	global_load_dwordx4 v[188:191], v245, s[84:85] nt
	s_add_u32 s84, s84, 0x4000
	s_addc_u32 s85, s85, 0
	global_load_dwordx4 v[192:195], v245, s[84:85] nt
	s_add_u32 s84, s84, 0x4000
	s_addc_u32 s85, s85, 0
	global_load_dwordx4 v[196:199], v245, s[84:85] nt
	s_add_u32 s84, s84, 0x4000
	s_addc_u32 s85, s85, 0
	global_load_dwordx4 v[200:203], v245, s[84:85] nt
	s_add_u32 s84, s84, 0x4000
	s_addc_u32 s85, s85, 0
	global_load_dwordx4 v[204:207], v245, s[84:85] nt
	s_add_u32 s84, s84, 0x4000
	s_addc_u32 s85, s85, 0
	global_load_dwordx4 v[208:211], v245, s[84:85] nt
	s_add_u32 s84, s84, 0x4000
	s_addc_u32 s85, s85, 0
	global_load_dwordx4 v[212:215], v245, s[84:85] nt
	s_add_u32 s84, s84, 0x4000
	s_addc_u32 s85, s85, 0
	global_load_dwordx4 v[216:219], v245, s[84:85] nt
	s_add_u32 s84, s84, 0x4000
	s_addc_u32 s85, s85, 0
	global_load_dwordx4 v[220:223], v245, s[84:85] nt
	s_add_u32 s84, s84, 0x4000
	s_addc_u32 s85, s85, 0
	global_load_dwordx4 v[224:227], v245, s[84:85] nt
	s_add_u32 s84, s84, 0x4000
	s_addc_u32 s85, s85, 0
	global_load_dwordx4 v[228:231], v245, s[84:85] nt
	s_add_u32 s84, s84, 0x4000
	s_addc_u32 s85, s85, 0
	global_load_dwordx4 v[232:235], v245, s[84:85] nt
	s_add_u32 s84, s84, 0x4000
	s_addc_u32 s85, s85, 0
	global_load_dwordx4 v[236:239], v245, s[84:85] nt
	s_add_u32 s84, s84, 0x4000
	s_addc_u32 s85, s85, 0
	global_load_dwordx4 v[240:243], v245, s[84:85] nt
